# v21_mainpro
# speedup vs baseline: 1.0074x; 1.0046x over previous
.LBB4_2:
	s_or_b64 exec, exec, s[2:3]
	v_lshlrev_b32_e32 v1, 2, v0
	global_load_dword v246, v1, s[14:15]
	s_ashr_i32 s5, s4, 31
	s_lshl_b64 s[4:5], s[4:5], 11
	s_movk_i32 s2, 0x80
	v_add_u32_e32 v247, 0x1ac00, v1
	s_add_u32 s8, s10, s4
	v_lshlrev_b32_e32 v62, 3, v0
	v_cmp_gt_u32_e64 s[2:3], s2, v0
	s_addc_u32 s9, s11, s5
	v_lshrrev_b32_e32 v1, 3, v0
	s_and_saveexec_b64 s[4:5], s[2:3]
	s_cbranch_execz .LBB4_4
	v_lshlrev_b32_e32 v68, 11, v1
	v_mov_b32_e32 v69, 0
	v_lshl_add_u64 v[2:3], s[8:9], 0, v[68:69]
	v_and_b32_e32 v68, 0x70, v210
	v_lshl_add_u64 v[82:83], v[2:3], 0, v[68:69]
	global_load_dwordx4 v[64:67], v[82:83], off offset:1920
	global_load_dwordx4 v[2:5], v[82:83], off offset:1792
	v_mul_u32_u24_e32 v63, 0x90, v1
	s_mov_b32 s10, 0x1a300
	v_add3_u32 v63, v63, v68, s10
	s_waitcnt vmcnt(1)
	ds_write_b128 v63, v[64:67]
.LBB4_4:
	s_or_b64 exec, exec, s[4:5]
	s_waitcnt vmcnt(0)
	ds_write_b32 v247, v246
	v_and_b32_e32 v62, 24, v62
	v_lshrrev_b32_e32 v200, 2, v0
	v_lshlrev_b32_e32 v201, 1, v62
	s_movk_i32 s4, 0x50
	v_mad_u32_u24 v62, v200, s4, v201
	v_add_u32_e32 v63, 0xa000, v62
	ds_write_b128 v62, v[10:13] offset:40960
	ds_write_b128 v62, v[14:17] offset:51200
	ds_write_b128 v62, v[58:61] offset:61440
	ds_write_b128 v63, v[34:37] offset:30720
	s_and_saveexec_b64 s[4:5], s[2:3]
	s_cbranch_execz .LBB4_6
	v_mul_u32_u24_e32 v10, 0x90, v1
	v_and_b32_e32 v11, 0x70, v210
	s_mov_b32 s10, 0x19a00
	v_add3_u32 v10, v10, v11, s10
	s_waitcnt vmcnt(0)
	ds_write_b128 v10, v[2:5]

	.amdhsa_kernel _Z6k_mainPKfS0_PKDF16_S0_PfPd
		.amdhsa_group_segment_fixed_size 111616
		.amdhsa_private_segment_fixed_size 0
		.amdhsa_kernarg_size 48
		.amdhsa_user_sgpr_count 2
		.amdhsa_user_sgpr_dispatch_ptr 0
		.amdhsa_user_sgpr_queue_ptr 0
		.amdhsa_user_sgpr_kernarg_segment_ptr 1
		.amdhsa_user_sgpr_dispatch_id 0
		.amdhsa_user_sgpr_kernarg_preload_length 0
		.amdhsa_user_sgpr_kernarg_preload_offset 0
		.amdhsa_user_sgpr_private_segment_size 0
		.amdhsa_uses_dynamic_stack 0
		.amdhsa_enable_private_segment 0
		.amdhsa_system_sgpr_workgroup_id_x 1
		.amdhsa_system_sgpr_workgroup_id_y 0
		.amdhsa_system_sgpr_workgroup_id_z 0
		.amdhsa_system_sgpr_workgroup_info 0
		.amdhsa_system_vgpr_workitem_id 0
		.amdhsa_next_free_vgpr 248
		.amdhsa_next_free_sgpr 96
		.amdhsa_accum_offset 248
		.amdhsa_reserve_vcc 1
		.amdhsa_float_round_mode_32 0
		.amdhsa_float_round_mode_16_64 0
		.amdhsa_float_denorm_mode_32 3
		.amdhsa_float_denorm_mode_16_64 3
		.amdhsa_dx10_clamp 1
		.amdhsa_ieee_mode 1
		.amdhsa_fp16_overflow 0
		.amdhsa_tg_split 0
		.amdhsa_exception_fp_ieee_invalid_op 0
		.amdhsa_exception_fp_denorm_src 0
		.amdhsa_exception_fp_ieee_div_zero 0
		.amdhsa_exception_fp_ieee_overflow 0
		.amdhsa_exception_fp_ieee_underflow 0
		.amdhsa_exception_fp_ieee_inexact 0
		.amdhsa_exception_int_div_zero 0
	.end_amdhsa_kernel

amdhsa.kernels:
  - .agpr_count:     16
    .args:
      - .actual_access:  read_only
        .address_space:  global
        .offset:         0
        .size:           8
        .value_kind:     global_buffer
      - .actual_access:  read_only
        .address_space:  global
        .offset:         8
        .size:           8
        .value_kind:     global_buffer
      - .actual_access:  read_only
        .address_space:  global
        .offset:         16
        .size:           8
        .value_kind:     global_buffer
      - .actual_access:  write_only
        .address_space:  global
        .offset:         24
        .size:           8
        .value_kind:     global_buffer
      - .actual_access:  write_only
        .address_space:  global
        .offset:         32
        .size:           8
        .value_kind:     global_buffer
      - .actual_access:  write_only
        .address_space:  global
        .offset:         40
        .size:           8
        .value_kind:     global_buffer
    .group_segment_fixed_size: 18944
    .kernarg_segment_align: 8
    .kernarg_segment_size: 48
    .language:       OpenCL C
    .language_version:
      - 2
      - 0
    .max_flat_workgroup_size: 256
    .name:           _Z9k_gemm_byPKfS0_S0_PfS1_Pd
    .private_segment_fixed_size: 0
    .sgpr_count:     22
    .sgpr_spill_count: 0
    .symbol:         _Z9k_gemm_byPKfS0_S0_PfS1_Pd.kd
    .uniform_work_group_size: 1
    .uses_dynamic_stack: false
    .vgpr_count:     168
    .vgpr_spill_count: 0
    .wavefront_size: 64
  - .agpr_count:     48
    .args:
      - .address_space:  global
        .offset:         0
        .size:           8
        .value_kind:     global_buffer
      - .address_space:  global
        .offset:         8
        .size:           8
        .value_kind:     global_buffer
      - .address_space:  global
        .offset:         16
        .size:           8
        .value_kind:     global_buffer
      - .address_space:  global
        .offset:         24
        .size:           8
        .value_kind:     global_buffer
      - .actual_access:  write_only
        .address_space:  global
        .offset:         32
        .size:           8
        .value_kind:     global_buffer
      - .offset:         40
        .size:           4
        .value_kind:     by_value
      - .actual_access:  read_only
        .address_space:  global
        .offset:         48
        .size:           8
        .value_kind:     global_buffer
      - .actual_access:  read_only
        .address_space:  global
        .offset:         56
        .size:           8
        .value_kind:     global_buffer
      - .actual_access:  read_only
        .address_space:  global
        .offset:         64
        .size:           8
        .value_kind:     global_buffer
      - .address_space:  global
        .offset:         72
        .size:           8
        .value_kind:     global_buffer
      - .offset:         80
        .size:           4
        .value_kind:     by_value
      - .actual_access:  write_only
        .address_space:  global
        .offset:         88
        .size:           8
        .value_kind:     global_buffer
      - .actual_access:  write_only
        .address_space:  global
        .offset:         96
        .size:           8
        .value_kind:     global_buffer
      - .actual_access:  write_only
        .address_space:  global
        .offset:         104
        .size:           8
        .value_kind:     global_buffer
    .group_segment_fixed_size: 139520
    .kernarg_segment_align: 8
    .kernarg_segment_size: 112
    .language:       OpenCL C
    .language_version:
      - 2
      - 0
    .max_flat_workgroup_size: 256
    .name:           _Z7k_chol2PfS_S_S_PdiPKfS2_S2_S_iS_PDF16_S_
    .private_segment_fixed_size: 0
    .sgpr_count:     106
    .sgpr_spill_count: 0
    .symbol:         _Z7k_chol2PfS_S_S_PdiPKfS2_S2_S_iS_PDF16_S_.kd
    .uniform_work_group_size: 1
    .uses_dynamic_stack: false
    .vgpr_count:     252
    .vgpr_spill_count: 0
    .wavefront_size: 64
  - .agpr_count:     16
    .args:
      - .actual_access:  read_only
        .address_space:  global
        .offset:         0
        .size:           8
        .value_kind:     global_buffer
      - .address_space:  global
        .offset:         8
        .size:           8
        .value_kind:     global_buffer
      - .address_space:  global
        .offset:         16
        .size:           8
        .value_kind:     global_buffer
      - .actual_access:  read_only
        .address_space:  global
        .offset:         24
        .size:           8
        .value_kind:     global_buffer
      - .actual_access:  write_only
        .address_space:  global
        .offset:         32
        .size:           8
        .value_kind:     global_buffer
      - .actual_access:  write_only
        .address_space:  global
        .offset:         40
        .size:           8
        .value_kind:     global_buffer
      - .actual_access:  write_only
        .address_space:  global
        .offset:         48
        .size:           8
        .value_kind:     global_buffer
    .group_segment_fixed_size: 79872
    .kernarg_segment_align: 8
    .kernarg_segment_size: 56
    .language:       OpenCL C
    .language_version:
      - 2
      - 0
    .max_flat_workgroup_size: 256
    .name:           _Z6k_tailPKfPfS1_S0_S1_PDF16_S1_
    .private_segment_fixed_size: 0
    .sgpr_count:     34
    .sgpr_spill_count: 0
    .symbol:         _Z6k_tailPKfPfS1_S0_S1_PDF16_S1_.kd
    .uniform_work_group_size: 1
    .uses_dynamic_stack: false
    .vgpr_count:     160
    .vgpr_spill_count: 0
    .wavefront_size: 64
  - .agpr_count:     0
    .args:
      - .actual_access:  read_only
        .address_space:  global
        .offset:         0
        .size:           8
        .value_kind:     global_buffer
      - .actual_access:  read_only
        .address_space:  global
        .offset:         8
        .size:           8
        .value_kind:     global_buffer
      - .actual_access:  read_only
        .address_space:  global
        .offset:         16
        .size:           8
        .value_kind:     global_buffer
      - .actual_access:  write_only
        .address_space:  global
        .offset:         24
        .size:           8
        .value_kind:     global_buffer
      - .actual_access:  write_only
        .address_space:  global
        .offset:         32
        .size:           8
        .value_kind:     global_buffer
      - .actual_access:  write_only
        .address_space:  global
        .offset:         40
        .size:           8
        .value_kind:     global_buffer
    .group_segment_fixed_size: 16896
    .kernarg_segment_align: 8
    .kernarg_segment_size: 48
    .language:       OpenCL C
    .language_version:
      - 2
      - 0
    .max_flat_workgroup_size: 256
    .name:           _Z6k_prepPKfS0_S0_PfPDF16_S1_
    .private_segment_fixed_size: 0
    .sgpr_count:     28
    .sgpr_spill_count: 0
    .symbol:         _Z6k_prepPKfS0_S0_PfPDF16_S1_.kd
    .uniform_work_group_size: 1
    .uses_dynamic_stack: false
    .vgpr_count:     150
    .vgpr_spill_count: 0
    .wavefront_size: 64
  - .agpr_count:     0
    .args:
      - .actual_access:  read_only
        .address_space:  global
        .offset:         0
        .size:           8
        .value_kind:     global_buffer
      - .actual_access:  read_only
        .address_space:  global
        .offset:         8
        .size:           8
        .value_kind:     global_buffer
      - .actual_access:  read_only
        .address_space:  global
        .offset:         16
        .size:           8
        .value_kind:     global_buffer
      - .actual_access:  read_only
        .address_space:  global
        .offset:         24
        .size:           8
        .value_kind:     global_buffer
      - .actual_access:  write_only
        .address_space:  global
        .offset:         32
        .size:           8
        .value_kind:     global_buffer
      - .actual_access:  write_only
        .address_space:  global
        .offset:         40
        .size:           8
        .value_kind:     global_buffer
    .group_segment_fixed_size: 111616
    .kernarg_segment_align: 8
    .kernarg_segment_size: 48
    .language:       OpenCL C
    .language_version:
      - 2
      - 0
    .max_flat_workgroup_size: 512
    .name:           _Z6k_mainPKfS0_PKDF16_S0_PfPd
    .private_segment_fixed_size: 0
    .sgpr_count:     25
    .sgpr_spill_count: 0
    .symbol:         _Z6k_mainPKfS0_PKDF16_S0_PfPd.kd
    .uniform_work_group_size: 1
    .uses_dynamic_stack: false
    .vgpr_count:     248
    .vgpr_spill_count: 0
    .wavefront_size: 64
  - .agpr_count:     0
    .args:
      - .actual_access:  read_only
        .address_space:  global
        .offset:         0
        .size:           8
        .value_kind:     global_buffer
      - .actual_access:  write_only
        .address_space:  global
        .offset:         8
        .size:           8
        .value_kind:     global_buffer
    .group_segment_fixed_size: 0
    .kernarg_segment_align: 8
    .kernarg_segment_size: 16
    .language:       OpenCL C
    .language_version:
      - 2
      - 0
    .max_flat_workgroup_size: 1024
    .name:           _Z7k_finalPKdPf
    .private_segment_fixed_size: 0
    .sgpr_count:     28
    .sgpr_spill_count: 0
    .symbol:         _Z7k_finalPKdPf.kd
    .uniform_work_group_size: 1
    .uses_dynamic_stack: false
    .vgpr_count:     60
    .vgpr_spill_count: 0
    .wavefront_size: 64
